# speedup vs baseline: 1.0033x; 1.0033x over previous
.LBB2_25:
	s_load_dwordx2 s[36:37], s[0:1], 0x30
	s_mov_b32 s38, 0
	v_and_b32_e32 v69, 15, v0
	s_and_b64 vcc, exec, s[2:3]
	s_cbranch_vccz .LBB2_53
	v_cmp_gt_i32_e32 vcc, 32, v35
	s_cmp_lg_u64 vcc, exec
	v_cmp_lt_i32_e64 s[2:3], v69, v35
	s_cbranch_scc0 .LBB2_38
	s_setprio 3
	v_mov_b32_e32 v3, 0
	v_mov_b32_e32 v6, v34
	v_mov_b32_e32 v7, 0
	v_mov_b32_e32 v8, 0
	s_and_saveexec_b64 s[4:5], s[2:3]
	s_cbranch_execz .LBB2_29
	v_add_u32_e32 v4, v36, v69
	v_ashrrev_i32_e32 v5, 31, v4
	v_lshl_add_u64 v[4:5], v[4:5], 4, s[30:31]
	global_load_dwordx4 v[6:9], v[4:5], off nt

.LBB2_33:
	s_or_b64 exec, exec, s[8:9]
	s_waitcnt vmcnt(0)
	v_or_b32_e32 v9, 16, v69
	v_lshlrev_b32_e32 v14, 2, v6
	v_lshl_add_u64 v[38:39], v[14:15], 2, s[28:29]
	v_lshlrev_b32_e32 v14, 2, v2
	v_lshl_add_u64 v[16:17], v[14:15], 2, s[28:29]
	v_lshlrev_b32_e32 v14, 2, v10
	v_lshl_add_u64 v[14:15], v[14:15], 2, s[28:29]
	global_load_dwordx3 v[30:32], v[38:39], off offset:4
	global_load_dwordx4 v[22:25], v[16:17], off
	global_load_dwordx4 v[26:29], v[14:15], off
	v_lshlrev_b32_e32 v14, 2, v34
	v_ashrrev_i32_e32 v15, 31, v14
	v_lshlrev_b64 v[14:15], 2, v[14:15]
	s_waitcnt lgkmcnt(0)
	v_lshl_add_u64 v[16:17], s[34:35], 0, v[14:15]
	v_lshl_add_u64 v[14:15], s[28:29], 0, v[14:15]
	global_load_dwordx4 v[18:21], v[16:17], off
	v_cvt_f32_f16_e32 v37, v7
	global_load_dwordx4 v[14:17], v[14:15], off
	global_load_dword v48, v[38:39], off
	s_movk_i32 s8, 0x410
	v_mul_lo_u32 v70, v41, s8
	v_lshlrev_b32_e32 v71, 4, v69
	s_mov_b32 s38, 1
	v_lshl_add_u32 v47, v69, 2, v70
	ds_write_b32 v47, v6 offset:768
	s_mov_b32 s21, s44
	ds_read_b96 v[62:64], v70 offset:768
	ds_read2_b32 v[66:67], v70 offset0:195 offset1:196
	ds_read_b32 v65, v70 offset:788
	s_waitcnt lgkmcnt(2)
	v_lshl_or_b32 v74, v62, 8, v71
	v_lshl_or_b32 v78, v63, 8, v71
	v_lshl_or_b32 v82, v64, 8, v71
	buffer_load_dwordx4 v[74:77], v74, s[20:23], 0 offen
	buffer_load_dwordx4 v[78:81], v78, s[20:23], 0 offen
	buffer_load_dwordx4 v[82:85], v82, s[20:23], 0 offen
	s_waitcnt lgkmcnt(0)
	v_lshl_or_b32 v86, v66, 8, v71
	v_lshl_or_b32 v90, v67, 8, v71
	v_lshl_or_b32 v50, v65, 8, v71
	buffer_load_dwordx4 v[86:89], v86, s[20:23], 0 offen
	buffer_load_dwordx4 v[90:93], v90, s[20:23], 0 offen
	buffer_load_dwordx4 v[50:53], v50, s[20:23], 0 offen
	v_mov_b32_e32 v5, 0xff800000
	v_mov_b32_e32 v13, 0xff800000
	s_and_saveexec_b64 s[8:9], s[2:3]
	s_cbranch_execz .LBB2_35
	s_waitcnt vmcnt(6)
	v_add_f32_e32 v13, v18, v48
	v_add_f32_e32 v13, v13, v37
	v_mul_f32_e32 v38, 0x3e4ccccd, v13
	v_cmp_lt_f32_e32 vcc, 0, v13
	s_nop 1
	v_cndmask_b32_e32 v13, v38, v13, vcc
.LBB2_35:
	s_or_b64 exec, exec, s[8:9]
	v_cvt_f32_i32_e32 v38, v35
	v_cvt_f32_f16_sdwa v40, v7 dst_sel:DWORD dst_unused:UNUSED_PAD src0_sel:WORD_1
	v_cvt_f32_f16_e32 v39, v3
	v_cvt_f32_f16_e32 v43, v11
	v_max_f32_e32 v7, 1.0, v38
	v_div_scale_f32 v38, s[8:9], v7, v7, 1.0
	v_rcp_f32_e32 v42, v38
	v_div_scale_f32 v44, vcc, 1.0, v7, 1.0
	s_waitcnt vmcnt(6)
	v_add_f32_e32 v22, v22, v18
	v_fma_f32 v45, -v38, v42, 1.0
	v_fmac_f32_e32 v42, v45, v42
	v_mul_f32_e32 v45, v44, v42
	v_fma_f32 v46, -v38, v45, v44
	v_fmac_f32_e32 v45, v46, v42
	v_fma_f32 v38, -v38, v45, v44
	v_add_f32_e32 v37, 0, v37
	v_add_f32_e32 v22, v22, v39
	v_add_f32_e32 v26, v26, v18
	v_div_fmas_f32 v38, v38, v42, v45
	v_cndmask_b32_e64 v37, 0, v37, s[2:3]
	v_mul_f32_e32 v42, 0x3e4ccccd, v22
	v_cmp_lt_f32_e32 vcc, 0, v22
	v_cndmask_b32_e64 v39, 0, v39, s[4:5]
	v_add_f32_e32 v26, v26, v43
	v_cndmask_b32_e32 v22, v42, v22, vcc
	v_add_f32_e32 v37, v37, v39
	v_mul_f32_e32 v39, 0x3e4ccccd, v26
	v_cmp_lt_f32_e32 vcc, 0, v26
	v_div_fixup_f32 v7, v38, v7, 1.0
	v_max_f32_e32 v38, v13, v13
	v_cndmask_b32_e32 v26, v39, v26, vcc
	v_cndmask_b32_e64 v39, 0, v43, s[6:7]
	v_max_f32_e32 v38, 0xff800000, v38
	v_cndmask_b32_e64 v22, v5, v22, s[4:5]
	v_cndmask_b32_e64 v26, v5, v26, s[6:7]
	v_add_f32_e32 v37, v37, v39
	v_max3_f32 v44, v38, v22, v26
	s_waitcnt vmcnt(6)
	v_mov_b32_e32 v42, v14
	v_add_f32_e32 v23, v23, v19
	v_add_f32_dpp v37, v37, v37 quad_perm:[1,0,3,2] row_mask:0xf bank_mask:0xf
	v_add_f32_e32 v24, v24, v20
	s_nop 0
	v_add_f32_dpp v37, v37, v37 quad_perm:[2,3,0,1] row_mask:0xf bank_mask:0xf
	s_nop 1
	v_add_f32_dpp v39, v37, v37 row_half_mirror row_mask:0xf bank_mask:0xf
	v_mov_b32_e32 v38, v18
	v_mov_b32_e32 v43, v39
	s_nop 0
	v_max_f32_dpp v18, v44, v44 quad_perm:[1,0,3,2] row_mask:0xf bank_mask:0xf
	v_mov_b32_dpp v43, v43 row_mirror row_mask:0xf bank_mask:0xf
	v_pk_add_f32 v[38:39], v[38:39], v[42:43]
	v_max_f32_dpp v18, v18, v18 quad_perm:[2,3,0,1] row_mask:0xf bank_mask:0xf
	v_fmac_f32_e32 v38, v7, v39
	v_mul_f32_e32 v14, 0x3e4ccccd, v38
	v_max_f32_dpp v18, v18, v18 row_half_mirror row_mask:0xf bank_mask:0xf
	v_cmp_lt_f32_e32 vcc, 0, v38
	v_cvt_f32_f16_sdwa v42, v11 dst_sel:DWORD dst_unused:UNUSED_PAD src0_sel:WORD_1
	s_nop 0
	v_cndmask_b32_e32 v14, v14, v38, vcc
	v_max_f32_dpp v37, v18, v18 row_mirror row_mask:0xf bank_mask:0xf
	v_max_f32_e32 v37, v37, v14
	v_sub_f32_e32 v13, v13, v37
	v_mul_f32_e32 v13, 0x3fb8aa3b, v13
	v_sub_f32_e32 v11, v22, v37
	v_exp_f32_e32 v13, v13
	v_mul_f32_e32 v11, 0x3fb8aa3b, v11
	v_sub_f32_e32 v18, v26, v37
	v_exp_f32_e32 v11, v11
	v_mul_f32_e32 v18, 0x3fb8aa3b, v18
	v_exp_f32_e32 v18, v18
	v_cvt_f32_f16_sdwa v39, v3 dst_sel:DWORD dst_unused:UNUSED_PAD src0_sel:WORD_1
	v_add_f32_e32 v3, 0, v13
	v_cndmask_b32_e64 v3, 0, v3, s[2:3]
	v_cndmask_b32_e64 v22, 0, v11, s[4:5]
	v_add_f32_e32 v3, v22, v3
	v_cndmask_b32_e64 v22, 0, v18, s[6:7]
	v_sub_f32_e32 v14, v14, v37
	v_add_f32_e32 v3, v22, v3
	v_mul_f32_e32 v14, 0x3fb8aa3b, v14
	v_exp_f32_e32 v37, v14
	v_add_f32_e32 v23, v23, v39
	v_mul_f32_e32 v26, 0x3e4ccccd, v23
	v_add_f32_dpp v3, v3, v3 quad_perm:[1,0,3,2] row_mask:0xf bank_mask:0xf
	v_cvt_f32_f16_e32 v38, v8
	s_nop 0
	v_add_f32_dpp v3, v3, v3 quad_perm:[2,3,0,1] row_mask:0xf bank_mask:0xf
	s_nop 1
	v_add_f32_dpp v3, v3, v3 row_half_mirror row_mask:0xf bank_mask:0xf
	s_nop 1
	v_add_f32_dpp v3, v3, v3 row_mirror row_mask:0xf bank_mask:0xf
	v_add_f32_e32 v14, v30, v19
	v_add_f32_e32 v14, v14, v40
	v_mul_f32_e32 v22, 0x3e4ccccd, v14
	v_cmp_lt_f32_e32 vcc, 0, v14
	v_add_f32_e32 v3, v37, v3
	v_add_f32_e32 v3, 0x24e69595, v3
	v_cndmask_b32_e32 v14, v22, v14, vcc
	v_cmp_lt_f32_e32 vcc, 0, v23
	v_add_f32_e32 v22, 0, v40
	v_cndmask_b32_e64 v22, 0, v22, s[2:3]
	v_cndmask_b32_e32 v23, v26, v23, vcc
	v_cndmask_b32_e64 v26, 0, v39, s[4:5]
	v_cndmask_b32_e64 v39, v5, v23, s[4:5]
	v_add_f32_e32 v23, v27, v19
	v_add_f32_e32 v23, v23, v42
	v_add_f32_e32 v22, v22, v26
	v_mul_f32_e32 v26, 0x3e4ccccd, v23
	v_cmp_lt_f32_e32 vcc, 0, v23
	v_cndmask_b32_e64 v30, v5, v14, s[2:3]
	v_max_f32_e32 v14, 0xff800000, v30
	v_cndmask_b32_e32 v23, v26, v23, vcc
	v_cndmask_b32_e64 v26, 0, v42, s[6:7]
	v_cndmask_b32_e64 v40, v5, v23, s[6:7]
	v_max3_f32 v42, v14, v39, v40
	v_add_f32_e32 v14, v22, v26
	v_mov_b32_e32 v26, v15
	v_rcp_f32_e32 v3, v3
	v_add_f32_dpp v14, v14, v14 quad_perm:[1,0,3,2] row_mask:0xf bank_mask:0xf
	s_nop 1
	v_add_f32_dpp v14, v14, v14 quad_perm:[2,3,0,1] row_mask:0xf bank_mask:0xf
	s_nop 1
	v_add_f32_dpp v23, v14, v14 row_half_mirror row_mask:0xf bank_mask:0xf
	v_mov_b32_e32 v27, v23
	v_mov_b32_e32 v22, v19
	s_nop 0
	v_mov_b32_dpp v27, v27 row_mirror row_mask:0xf bank_mask:0xf
	v_pk_add_f32 v[14:15], v[22:23], v[26:27]
	v_mul_f32_e32 v22, v37, v3
	v_fmac_f32_e32 v14, v7, v15
	v_mul_f32_e32 v15, 0x3e4ccccd, v14
	v_cmp_lt_f32_e32 vcc, 0, v14
	v_cvt_f32_f16_e32 v27, v4
	v_add_f32_e32 v24, v24, v27
	v_cndmask_b32_e32 v14, v15, v14, vcc
	v_cndmask_b32_e64 v27, 0, v27, s[4:5]
	s_nop 0
	v_max_f32_dpp v15, v42, v42 quad_perm:[1,0,3,2] row_mask:0xf bank_mask:0xf
	s_nop 1
	v_max_f32_dpp v15, v15, v15 quad_perm:[2,3,0,1] row_mask:0xf bank_mask:0xf
	s_nop 1
	v_max_f32_dpp v15, v15, v15 row_half_mirror row_mask:0xf bank_mask:0xf
	s_nop 1
	v_max_f32_dpp v19, v15, v15 row_mirror row_mask:0xf bank_mask:0xf
	v_max_f32_e32 v15, v19, v14
	v_sub_f32_e32 v19, v30, v15
	v_mul_f32_e32 v19, 0x3fb8aa3b, v19
	v_exp_f32_e32 v23, v19
	v_sub_f32_e32 v19, v39, v15
	v_mul_f32_e32 v19, 0x3fb8aa3b, v19
	v_sub_f32_e32 v26, v40, v15
	v_exp_f32_e32 v19, v19
	v_mul_f32_e32 v26, 0x3fb8aa3b, v26
	v_exp_f32_e32 v26, v26
	v_add_f32_e32 v37, 0, v23
	v_cndmask_b32_e64 v37, 0, v37, s[2:3]
	v_cndmask_b32_e64 v39, 0, v19, s[4:5]
	v_add_f32_e32 v37, v39, v37
	v_cndmask_b32_e64 v39, 0, v26, s[6:7]
	v_sub_f32_e32 v14, v14, v15
	v_add_f32_e32 v37, v39, v37
	v_mul_f32_e32 v14, 0x3fb8aa3b, v14
	v_exp_f32_e32 v39, v14
	v_cvt_f32_f16_e32 v30, v12
	s_nop 0
	v_add_f32_dpp v14, v37, v37 quad_perm:[1,0,3,2] row_mask:0xf bank_mask:0xf
	s_nop 1
	v_add_f32_dpp v14, v14, v14 quad_perm:[2,3,0,1] row_mask:0xf bank_mask:0xf
	s_nop 1
	v_add_f32_dpp v14, v14, v14 row_half_mirror row_mask:0xf bank_mask:0xf
	s_nop 1
	v_add_f32_dpp v37, v14, v14 row_mirror row_mask:0xf bank_mask:0xf
	v_add_f32_e32 v14, v31, v20
	v_add_f32_e32 v14, v14, v38
	v_mul_f32_e32 v15, 0x3e4ccccd, v14
	v_cmp_lt_f32_e32 vcc, 0, v14
	v_mul_f32_e32 v31, 0x3e4ccccd, v24
	s_nop 0
	v_cndmask_b32_e32 v14, v15, v14, vcc
	v_cmp_lt_f32_e32 vcc, 0, v24
	v_add_f32_e32 v15, 0, v38
	v_cndmask_b32_e64 v15, 0, v15, s[2:3]
	v_cndmask_b32_e32 v24, v31, v24, vcc
	v_cndmask_b32_e64 v38, v5, v24, s[4:5]
	v_add_f32_e32 v24, v28, v20
	v_add_f32_e32 v24, v24, v30
	v_add_f32_e32 v15, v15, v27
	v_mul_f32_e32 v27, 0x3e4ccccd, v24
	v_cmp_lt_f32_e32 vcc, 0, v24
	v_cndmask_b32_e64 v40, v5, v14, s[2:3]
	v_max_f32_e32 v14, 0xff800000, v40
	v_cndmask_b32_e32 v24, v27, v24, vcc
	v_cndmask_b32_e64 v27, 0, v30, s[6:7]
	v_cndmask_b32_e64 v28, v5, v24, s[6:7]
	v_max3_f32 v24, v14, v38, v28
	v_add_f32_e32 v14, v15, v27
	v_mov_b32_e32 v30, v16
	s_nop 0
	v_add_f32_dpp v14, v14, v14 quad_perm:[1,0,3,2] row_mask:0xf bank_mask:0xf
	s_nop 1
	v_add_f32_dpp v14, v14, v14 quad_perm:[2,3,0,1] row_mask:0xf bank_mask:0xf
	s_nop 1
	v_add_f32_dpp v15, v14, v14 row_half_mirror row_mask:0xf bank_mask:0xf
	v_mov_b32_e32 v31, v15
	v_mov_b32_e32 v14, v20
	s_nop 0
	v_mov_b32_dpp v31, v31 row_mirror row_mask:0xf bank_mask:0xf
	v_pk_add_f32 v[14:15], v[14:15], v[30:31]
	s_nop 0
	v_fmac_f32_e32 v14, v7, v15
	v_mul_f32_e32 v15, 0x3e4ccccd, v14
	v_cmp_lt_f32_e32 vcc, 0, v14
	s_nop 1
	v_cndmask_b32_e32 v14, v15, v14, vcc
	v_cmp_eq_u32_e32 vcc, v33, v35
	s_nop 0
	v_max_f32_dpp v15, v24, v24 quad_perm:[1,0,3,2] row_mask:0xf bank_mask:0xf
	s_nop 1
	v_max_f32_dpp v15, v15, v15 quad_perm:[2,3,0,1] row_mask:0xf bank_mask:0xf
	s_nop 1
	v_max_f32_dpp v15, v15, v15 row_half_mirror row_mask:0xf bank_mask:0xf
	s_nop 1
	v_max_f32_dpp v16, v15, v15 row_mirror row_mask:0xf bank_mask:0xf
	v_max_f32_e32 v15, v16, v14
	v_sub_f32_e32 v16, v40, v15
	v_mul_f32_e32 v16, 0x3fb8aa3b, v16
	v_sub_f32_e32 v20, v38, v15
	v_exp_f32_e32 v24, v16
	v_mul_f32_e32 v20, 0x3fb8aa3b, v20
	v_sub_f32_e32 v28, v28, v15
	v_exp_f32_e32 v20, v20
	v_mul_f32_e32 v28, 0x3fb8aa3b, v28
	v_add_f32_e32 v16, v39, v37
	v_exp_f32_e32 v37, v28
	v_add_f32_e32 v16, 0x24e69595, v16
	v_rcp_f32_e32 v27, v16
	v_add_f32_e32 v16, 0, v24
	v_cndmask_b32_e64 v16, 0, v16, s[2:3]
	v_cndmask_b32_e64 v28, 0, v20, s[4:5]
	v_add_f32_e32 v16, v28, v16
	v_cndmask_b32_e64 v28, 0, v37, s[6:7]
	v_sub_f32_e32 v14, v14, v15
	v_add_f32_e32 v16, v28, v16
	v_mul_f32_e32 v14, 0x3fb8aa3b, v14
	v_exp_f32_e32 v28, v14
	v_mul_f32_e32 v30, v39, v27
	s_nop 0
	v_add_f32_dpp v14, v16, v16 quad_perm:[1,0,3,2] row_mask:0xf bank_mask:0xf
	s_nop 1
	v_add_f32_dpp v14, v14, v14 quad_perm:[2,3,0,1] row_mask:0xf bank_mask:0xf
	s_nop 1
	v_add_f32_dpp v14, v14, v14 row_half_mirror row_mask:0xf bank_mask:0xf
	s_nop 1
	v_add_f32_dpp v14, v14, v14 row_mirror row_mask:0xf bank_mask:0xf
	v_add_f32_e32 v14, v28, v14
	v_add_f32_e32 v14, 0x24e69595, v14
	v_rcp_f32_e32 v31, v14
	v_cndmask_b32_e32 v14, 0, v22, vcc
	v_cndmask_b32_e32 v15, 0, v30, vcc
	v_mul_f32_e32 v33, v28, v31
	v_cndmask_b32_e32 v16, 0, v33, vcc
	v_mov_b32_e32 v28, 0
	s_and_saveexec_b64 s[10:11], s[6:7]
	s_cbranch_execz .LBB2_37
	v_cvt_f32_f16_sdwa v28, v12 dst_sel:DWORD dst_unused:UNUSED_PAD src0_sel:WORD_1
	v_add_f32_e32 v5, v29, v21
	v_mul_f32_e32 v16, v37, v31
	v_mul_f32_e32 v15, v26, v27
	v_add_f32_e32 v5, v5, v28
	v_mul_f32_e32 v12, 0x3e4ccccd, v5
	v_cmp_lt_f32_e64 s[8:9], 0, v5
	v_mul_f32_e32 v14, v18, v3
	s_nop 0
	v_cndmask_b32_e64 v5, v12, v5, s[8:9]

.LBB2_57:
	s_endpgm
	s_nop 0
	s_nop 0
	s_nop 0
	s_nop 0
	s_nop 0
	s_nop 0
	s_nop 0
	s_nop 0
	s_nop 0
	s_nop 0
	s_nop 0
	s_nop 0
	s_nop 0
	s_nop 0
	s_endpgm
